# idle waves touch the next phase's code bytes (56 KB ahead of PC) with global loads while the grid barrier runs, to warm L2 for instruction fetch; on top of v040
# speedup vs baseline: 1.0012x; 1.0012x over previous
.LBB0_238:
	s_cmp_gt_i32 s29, 1
	s_cselect_b64 s[0:1], -1, 0
	s_and_b64 s[0:1], s[12:13], s[0:1]
	s_andn2_b64 vcc, exec, s[0:1]
	s_cbranch_vccnz .LBB0_293
	s_mov_b64 s[6:7], s[74:75]
	s_getreg_b32 s0, hwreg(HW_REG_XCC_ID, 0, 4)
	s_waitcnt vmcnt(0)
	s_waitcnt lgkmcnt(0)
	s_barrier
	v_readfirstlane_b32 s2, v0
	s_cmp_lt_u32 s2, 64
	s_cbranch_scc1 .Ltch0
	s_getpc_b64 s[2:3]
	v_lshlrev_b32_e32 v1, 7, v0
	s_sub_u32 s2, s2, 0x2000
	s_subb_u32 s3, s3, 0
	global_load_dword v1, v1, s[2:3]
	s_waitcnt vmcnt(0)
.Ltch0:
	s_mov_b64 s[4:5], exec
	v_readlane_b32 s2, v254, 1
	v_readlane_b32 s3, v254, 2
	s_and_b64 s[2:3], s[4:5], s[2:3]
	s_mov_b64 exec, s[2:3]
	s_cbranch_execz .LBB0_292
	s_add_i32 s1, 0, 0x20000
	v_mov_b32_e32 v1, s1
	s_load_dwordx2 s[6:7], s[6:7], 0xd8
	s_waitcnt vmcnt(0) expcnt(0) lgkmcnt(0)
	ds_read_b32 v3, v1
	s_add_i32 s1, 0, 0x20004
	v_mov_b32_e32 v1, s1
	ds_read_b32 v1, v1
	s_and_b32 s0, s0, 15
	s_waitcnt lgkmcnt(1)
	v_cmp_ne_u32_e32 vcc, 0, v3
	s_cbranch_vccnz .LBB0_256
	s_add_u32 s8, s6, 0x4200
	s_addc_u32 s9, s7, 0
	s_add_u32 s10, s6, 0x4400
	s_addc_u32 s11, s7, 0
	s_add_u32 s12, s6, 0x4500
	s_addc_u32 s13, s7, 0
	s_add_u32 s14, s6, 0x4600
	s_addc_u32 s15, s7, 0
	s_add_u32 s16, s6, 0x4700
	s_addc_u32 s17, s7, 0
	s_add_u32 s18, s6, 0x4800
	s_addc_u32 s19, s7, 0
	s_add_u32 s22, s6, 0x4900
	s_addc_u32 s23, s7, 0
	s_add_u32 s24, s6, 0x4a00
	s_addc_u32 s25, s7, 0
	s_add_u32 s26, s6, 0x4b00
	s_addc_u32 s27, s7, 0
	s_add_u32 s30, s6, 0x4c00
	s_addc_u32 s31, s7, 0
	s_add_u32 s34, s6, 0x4d00
	s_addc_u32 s35, s7, 0
	s_add_u32 s36, s6, 0x4e00
	s_addc_u32 s37, s7, 0
	s_add_u32 s38, s6, 0x4f00
	s_addc_u32 s39, s7, 0
	s_add_u32 s40, s6, 0x5000
	s_addc_u32 s41, s7, 0
	s_load_dwordx2 s[2:3], s[74:75], 0x148
	s_load_dword s1, s[74:75], 0x150
	s_add_u32 s42, s6, 0x5100
	s_addc_u32 s43, s7, 0
	s_add_u32 s44, s6, 0x5200
	s_addc_u32 s45, s7, 0
	s_waitcnt lgkmcnt(0)
	s_mul_i32 s2, s3, s2
	s_add_u32 s46, s6, 0x5300
	s_mul_i32 s1, s2, s1
	s_addc_u32 s47, s7, 0
	s_mov_b32 s2, 1
	v_mov_b32_e32 v17, 0
	s_branch .LBB0_243

.LBB0_410:
	s_add_i32 s36, s84, 1
	s_cmp_lt_i32 s36, s29
	s_cselect_b64 s[4:5], -1, 0
	s_and_b64 s[6:7], s[12:13], s[4:5]
	s_andn2_b64 vcc, exec, s[6:7]
	s_cbranch_vccnz .LBB0_464
	s_waitcnt lgkmcnt(0)
	s_mov_b64 s[8:9], s[74:75]
	s_getreg_b32 s10, hwreg(HW_REG_XCC_ID, 0, 4)
	s_waitcnt vmcnt(0)
	s_waitcnt vmcnt(63) expcnt(7) lgkmcnt(15)
	s_barrier
	v_readfirstlane_b32 s12, v0
	s_cmp_lt_u32 s12, 64
	s_cbranch_scc1 .Ltch1
	s_getpc_b64 s[12:13]
	v_lshlrev_b32_e32 v1, 7, v0
	s_sub_u32 s12, s12, 0x2000
	s_subb_u32 s13, s13, 0
	global_load_dword v1, v1, s[12:13]
	s_waitcnt vmcnt(0)
.Ltch1:
	s_mov_b64 s[6:7], exec
	v_readlane_b32 s12, v254, 1
	v_readlane_b32 s13, v254, 2
	s_and_b64 s[12:13], s[6:7], s[12:13]
	s_mov_b64 exec, s[12:13]
	s_cbranch_execz .LBB0_463
	v_readlane_b32 s11, v254, 15
	s_load_dwordx2 s[8:9], s[8:9], 0xd8
	s_waitcnt vmcnt(0) expcnt(0) lgkmcnt(0)
	v_mov_b32_e32 v1, s11
	ds_read_b32 v4, v1
	v_readlane_b32 s11, v254, 16
	s_and_b32 s62, s10, 15
	s_waitcnt lgkmcnt(0)
	v_cmp_ne_u32_e32 vcc, 0, v4
	v_mov_b32_e32 v1, s11
	ds_read_b32 v2, v1
	s_cbranch_vccnz .LBB0_427
	v_readlane_b32 s10, v254, 3
	v_readlane_b32 s11, v254, 4
	s_load_dwordx2 s[14:15], s[10:11], 0x0
	s_load_dword s13, s[10:11], 0x8
	s_add_u32 s10, s8, 0x4200
	s_addc_u32 s11, s9, 0
	s_add_u32 s12, s8, 0x4400
	s_waitcnt lgkmcnt(0)
	s_mul_i32 s63, s15, s14
	s_mul_i32 s63, s63, s13
	s_addc_u32 s13, s9, 0
	s_add_u32 s14, s8, 0x4500
	s_addc_u32 s15, s9, 0
	s_add_u32 s16, s8, 0x4600
	s_addc_u32 s17, s9, 0
	s_add_u32 s18, s8, 0x4700
	s_addc_u32 s19, s9, 0
	s_add_u32 s22, s8, 0x4800
	s_addc_u32 s23, s9, 0
	s_add_u32 s24, s8, 0x4900
	s_addc_u32 s25, s9, 0
	s_add_u32 s26, s8, 0x4a00
	s_addc_u32 s27, s9, 0
	s_add_u32 s34, s8, 0x4b00
	s_addc_u32 s35, s9, 0
	s_add_u32 s38, s8, 0x4c00
	s_addc_u32 s39, s9, 0
	s_add_u32 s40, s8, 0x4d00
	s_addc_u32 s41, s9, 0
	s_add_u32 s42, s8, 0x4e00
	s_addc_u32 s43, s9, 0
	s_add_u32 s44, s8, 0x4f00
	s_addc_u32 s45, s9, 0
	s_add_u32 s46, s8, 0x5000
	s_addc_u32 s47, s9, 0
	s_add_u32 s48, s8, 0x5100
	s_addc_u32 s49, s9, 0
	s_add_u32 s50, s8, 0x5200
	s_addc_u32 s51, s9, 0
	s_add_u32 s52, s8, 0x5300
	s_addc_u32 s53, s9, 0
	s_mov_b32 s64, 1
	s_branch .LBB0_415

.LBB0_686:
	s_add_i32 s36, s84, 2
	s_cmp_lt_i32 s36, s29
	s_cselect_b64 s[4:5], -1, 0
	s_and_b64 s[6:7], s[18:19], s[4:5]
	s_mov_b32 s85, s84
	s_andn2_b64 vcc, exec, s[6:7]
	s_cbranch_vccnz .LBB0_740
	s_waitcnt lgkmcnt(0)
	s_mov_b64 s[8:9], s[74:75]
	s_getreg_b32 s10, hwreg(HW_REG_XCC_ID, 0, 4)
	s_waitcnt vmcnt(0)
	s_waitcnt vmcnt(0)
	s_barrier
	v_readfirstlane_b32 s12, v0
	s_cmp_lt_u32 s12, 64
	s_cbranch_scc1 .Ltch2
	s_getpc_b64 s[12:13]
	v_lshlrev_b32_e32 v1, 7, v0
	s_sub_u32 s12, s12, 0x2000
	s_subb_u32 s13, s13, 0
	global_load_dword v1, v1, s[12:13]
	s_waitcnt vmcnt(0)

.LBB0_817:
	s_add_i32 s36, s85, 3
	s_cmp_lt_i32 s36, s29
	s_cselect_b64 s[4:5], -1, 0
	s_and_b64 s[6:7], s[14:15], s[4:5]
	s_andn2_b64 vcc, exec, s[6:7]
	s_cbranch_vccnz .LBB0_871
	s_waitcnt lgkmcnt(0)
	s_mov_b64 s[8:9], s[74:75]
	s_getreg_b32 s10, hwreg(HW_REG_XCC_ID, 0, 4)
	s_waitcnt vmcnt(0)
	s_waitcnt vmcnt(0)
	s_barrier
	v_readfirstlane_b32 s12, v0
	s_cmp_lt_u32 s12, 64
	s_cbranch_scc1 .Ltch3
	s_getpc_b64 s[12:13]
	v_lshlrev_b32_e32 v1, 7, v0
	s_sub_u32 s12, s12, 0x2000
	s_subb_u32 s13, s13, 0
	global_load_dword v1, v1, s[12:13]
	s_waitcnt vmcnt(0)
.Ltch3:
	s_mov_b64 s[6:7], exec
	v_readlane_b32 s12, v254, 1
	v_readlane_b32 s13, v254, 2
	s_and_b64 s[12:13], s[6:7], s[12:13]
	s_mov_b64 exec, s[12:13]
	s_cbranch_execz .LBB0_870
	v_readlane_b32 s11, v254, 15
	s_load_dwordx2 s[8:9], s[8:9], 0xd8
	s_waitcnt vmcnt(0) expcnt(0) lgkmcnt(0)
	v_mov_b32_e32 v1, s11
	ds_read_b32 v4, v1
	v_readlane_b32 s11, v254, 16
	s_and_b32 s62, s10, 15
	s_waitcnt lgkmcnt(0)
	v_cmp_ne_u32_e32 vcc, 0, v4
	v_mov_b32_e32 v1, s11
	ds_read_b32 v2, v1
	s_cbranch_vccnz .LBB0_834
	v_readlane_b32 s10, v254, 3
	v_readlane_b32 s11, v254, 4
	s_load_dwordx2 s[14:15], s[10:11], 0x0
	s_load_dword s13, s[10:11], 0x8
	s_add_u32 s10, s8, 0x4200
	s_addc_u32 s11, s9, 0
	s_add_u32 s12, s8, 0x4400
	s_waitcnt lgkmcnt(0)
	s_mul_i32 s63, s15, s14
	s_mul_i32 s63, s63, s13
	s_addc_u32 s13, s9, 0
	s_add_u32 s14, s8, 0x4500
	s_addc_u32 s15, s9, 0
	s_add_u32 s16, s8, 0x4600
	s_addc_u32 s17, s9, 0
	s_add_u32 s18, s8, 0x4700
	s_addc_u32 s19, s9, 0
	s_add_u32 s22, s8, 0x4800
	s_addc_u32 s23, s9, 0
	s_add_u32 s24, s8, 0x4900
	s_addc_u32 s25, s9, 0
	s_add_u32 s26, s8, 0x4a00
	s_addc_u32 s27, s9, 0
	s_add_u32 s34, s8, 0x4b00
	s_addc_u32 s35, s9, 0
	s_add_u32 s38, s8, 0x4c00
	s_addc_u32 s39, s9, 0
	s_add_u32 s40, s8, 0x4d00
	s_addc_u32 s41, s9, 0
	s_add_u32 s42, s8, 0x4e00
	s_addc_u32 s43, s9, 0
	s_add_u32 s44, s8, 0x4f00
	s_addc_u32 s45, s9, 0
	s_add_u32 s46, s8, 0x5000
	s_addc_u32 s47, s9, 0
	s_add_u32 s48, s8, 0x5100
	s_addc_u32 s49, s9, 0
	s_add_u32 s50, s8, 0x5200
	s_addc_u32 s51, s9, 0
	s_add_u32 s52, s8, 0x5300
	s_addc_u32 s53, s9, 0
	s_mov_b32 s66, 1
	s_branch .LBB0_822

.LBB0_1055:
	s_add_i32 s36, s85, 4
	s_cmp_lt_i32 s36, s29
	s_cselect_b64 s[4:5], -1, 0
	s_and_b64 s[6:7], s[6:7], s[4:5]
	s_andn2_b64 vcc, exec, s[6:7]
	s_cbranch_vccnz .LBB0_1109
	s_waitcnt lgkmcnt(0)
	s_mov_b64 s[8:9], s[74:75]
	s_getreg_b32 s10, hwreg(HW_REG_XCC_ID, 0, 4)
	s_waitcnt vmcnt(0)
	s_waitcnt vmcnt(0)
	s_barrier
	v_readfirstlane_b32 s12, v0
	s_cmp_lt_u32 s12, 64
	s_cbranch_scc1 .Ltch4
	s_getpc_b64 s[12:13]
	v_lshlrev_b32_e32 v1, 7, v0
	s_sub_u32 s12, s12, 0x2000
	s_subb_u32 s13, s13, 0
	global_load_dword v1, v1, s[12:13]
	s_waitcnt vmcnt(0)

.LBB0_1132:
	s_add_i32 s36, s85, 5
	s_cmp_lt_i32 s36, s29
	s_cselect_b64 s[4:5], -1, 0
	s_and_b64 s[6:7], s[6:7], s[4:5]
	s_andn2_b64 vcc, exec, s[6:7]
	s_cbranch_vccnz .LBB0_1186
	s_waitcnt lgkmcnt(0)
	s_mov_b64 s[8:9], s[74:75]
	s_getreg_b32 s10, hwreg(HW_REG_XCC_ID, 0, 4)
	s_waitcnt vmcnt(0)
	s_waitcnt vmcnt(0)
	s_barrier
	v_readfirstlane_b32 s12, v0
	s_cmp_lt_u32 s12, 64
	s_cbranch_scc1 .Ltch5
	s_getpc_b64 s[12:13]
	v_lshlrev_b32_e32 v1, 7, v0
	s_sub_u32 s12, s12, 0x2000
	s_subb_u32 s13, s13, 0
	global_load_dword v1, v1, s[12:13]
	s_waitcnt vmcnt(0)

.LBB0_1206:
	s_add_i32 s36, s85, 6
	s_cmp_lt_i32 s36, s29
	s_cselect_b64 s[4:5], -1, 0
	s_and_b64 s[6:7], s[6:7], s[4:5]
	s_andn2_b64 vcc, exec, s[6:7]
	s_cbranch_vccnz .LBB0_1260
	s_waitcnt lgkmcnt(0)
	s_mov_b64 s[8:9], s[74:75]
	s_getreg_b32 s10, hwreg(HW_REG_XCC_ID, 0, 4)
	s_waitcnt vmcnt(0)
	s_waitcnt vmcnt(0)
	s_barrier
	v_readfirstlane_b32 s12, v0
	s_cmp_lt_u32 s12, 64
	s_cbranch_scc1 .Ltch6
	s_getpc_b64 s[12:13]
	v_lshlrev_b32_e32 v1, 7, v0
	s_sub_u32 s12, s12, 0x2000
	s_subb_u32 s13, s13, 0
	global_load_dword v1, v1, s[12:13]
	s_waitcnt vmcnt(0)

.LBB0_1346:
	s_add_i32 s36, s85, 7
	s_cmp_lt_i32 s36, s29
	s_cselect_b64 s[4:5], -1, 0
	s_and_b64 s[6:7], s[38:39], s[4:5]
	s_andn2_b64 vcc, exec, s[6:7]
	s_cbranch_vccnz .LBB0_1400
	s_waitcnt lgkmcnt(0)
	s_mov_b64 s[8:9], s[74:75]
	s_getreg_b32 s10, hwreg(HW_REG_XCC_ID, 0, 4)
	s_waitcnt vmcnt(0)
	s_waitcnt vmcnt(0)
	s_barrier
	v_readfirstlane_b32 s12, v0
	s_cmp_lt_u32 s12, 64
	s_cbranch_scc1 .Ltch7
	s_getpc_b64 s[12:13]
	v_lshlrev_b32_e32 v1, 7, v0
	s_sub_u32 s12, s12, 0x2000
	s_subb_u32 s13, s13, 0
	global_load_dword v1, v1, s[12:13]
	s_waitcnt vmcnt(0)

.LBB0_1427:
	s_add_i32 s66, s85, 8
	s_cmp_lt_i32 s66, s29
	s_cselect_b64 s[6:7], -1, 0
	s_and_b64 s[6:7], s[12:13], s[6:7]
	s_andn2_b64 vcc, exec, s[6:7]
	s_cbranch_vccnz .LBB0_1481
	s_mov_b64 s[8:9], s[74:75]
	s_getreg_b32 s10, hwreg(HW_REG_XCC_ID, 0, 4)
	s_waitcnt vmcnt(0)
	s_waitcnt vmcnt(0)
	s_barrier
	v_readfirstlane_b32 s14, v0
	s_cmp_lt_u32 s14, 64
	s_cbranch_scc1 .Ltch8
	s_getpc_b64 s[14:15]
	v_lshlrev_b32_e32 v1, 7, v0
	s_sub_u32 s14, s14, 0x2000
	s_subb_u32 s15, s15, 0
	global_load_dword v1, v1, s[14:15]
	s_waitcnt vmcnt(0)
.Ltch8:
	s_mov_b64 s[6:7], exec
	v_readlane_b32 s14, v254, 1
	v_readlane_b32 s15, v254, 2
	s_and_b64 s[14:15], s[6:7], s[14:15]
	s_mov_b64 exec, s[14:15]
	s_cbranch_execz .LBB0_1480
	v_readlane_b32 s11, v254, 15
	s_load_dwordx2 s[8:9], s[8:9], 0xd8
	s_waitcnt vmcnt(0) expcnt(0) lgkmcnt(0)
	v_mov_b32_e32 v1, s11
	ds_read_b32 v4, v1
	v_readlane_b32 s11, v254, 16
	s_and_b32 s36, s10, 15
	s_waitcnt lgkmcnt(0)
	v_cmp_ne_u32_e32 vcc, 0, v4
	v_mov_b32_e32 v1, s11
	ds_read_b32 v2, v1
	s_cbranch_vccnz .LBB0_1444
	v_readlane_b32 s10, v254, 3
	v_readlane_b32 s11, v254, 4
	s_load_dwordx2 s[16:17], s[10:11], 0x0
	s_load_dword s15, s[10:11], 0x8
	s_add_u32 s10, s8, 0x4200
	s_addc_u32 s11, s9, 0
	s_add_u32 s14, s8, 0x4400
	s_waitcnt lgkmcnt(0)
	s_mul_i32 s64, s17, s16
	s_mul_i32 s64, s64, s15
	s_addc_u32 s15, s9, 0
	s_add_u32 s16, s8, 0x4500
	s_addc_u32 s17, s9, 0
	s_add_u32 s18, s8, 0x4600
	s_addc_u32 s19, s9, 0
	s_add_u32 s22, s8, 0x4700
	s_addc_u32 s23, s9, 0
	s_add_u32 s24, s8, 0x4800
	s_addc_u32 s25, s9, 0
	s_add_u32 s26, s8, 0x4900
	s_addc_u32 s27, s9, 0
	s_add_u32 s34, s8, 0x4a00
	s_addc_u32 s35, s9, 0
	s_add_u32 s38, s8, 0x4b00
	s_addc_u32 s39, s9, 0
	s_add_u32 s40, s8, 0x4c00
	s_addc_u32 s41, s9, 0
	s_add_u32 s42, s8, 0x4d00
	s_addc_u32 s43, s9, 0
	s_add_u32 s44, s8, 0x4e00
	s_addc_u32 s45, s9, 0
	s_add_u32 s46, s8, 0x4f00
	s_addc_u32 s47, s9, 0
	s_add_u32 s48, s8, 0x5000
	s_addc_u32 s49, s9, 0
	s_add_u32 s50, s8, 0x5100
	s_addc_u32 s51, s9, 0
	s_add_u32 s52, s8, 0x5200
	s_addc_u32 s53, s9, 0
	s_add_u32 s54, s8, 0x5300
	s_addc_u32 s55, s9, 0
	s_mov_b32 s65, 1
	s_branch .LBB0_1432
